# v9 + GEMM prologues: K-tile 1 staging loads issued before the wait for K-tile 0 (vmcnt(2)+barrier moved behind them, recounted to vmcnt(8)) so the two cold fetches overlap
# speedup vs baseline: 1.0027x; 1.0027x over previous
.LBB0_165:
	v_and_b32_e32 v11, 15, v1
	v_bfe_u32 v10, v1, 4, 2
	v_lshl_or_b32 v1, s8, 6, v11
	v_lshlrev_b32_e32 v8, 4, v10
	v_lshlrev_b32_e32 v13, 2, v1
	s_and_b32 s16, s50, 3
	v_lshl_or_b32 v8, v11, 6, v8
	s_lshl_b32 s14, s8, 13
	v_and_b32_e32 v9, 32, v13
	s_waitcnt vmcnt(0)
	v_bitop3_b32 v14, v8, s14, v9 bitop3:0xde
	s_lshl_b32 s14, s16, 12
	s_and_b64 s[38:39], s[40:41], exec
	s_cselect_b32 s75, 0, 2
	s_add_u32 s84, s42, 0x30100000
	s_addc_u32 s85, s43, 0
	s_add_u32 s17, s42, 0x3a100000
	s_addc_u32 s26, s43, 0
	s_and_b64 s[38:39], s[40:41], exec
	v_lshlrev_b32_e32 v15, 2, v11
	s_cselect_b32 s47, s26, 0
	s_cselect_b32 s46, s17, 0
	s_add_u32 s38, s64, 0x8000
	v_mov_b32_e32 v151, v115
	v_and_b32_e32 v9, 32, v15
	s_addc_u32 s39, s65, 0
	v_bitop3_b32 v182, v8, s14, v9 bitop3:0xde
	s_add_i32 m0, s37, 0x18000
	v_lshl_add_u64 v[8:9], s[38:39], 0, v[150:151]
	v_mov_b32_e32 v155, v115
	global_load_lds_dwordx4 v[8:9], off
	s_add_i32 m0, s37, 0x1a000
	v_lshl_add_u64 v[8:9], s[38:39], 0, v[154:155]
	s_add_u32 s38, s62, 0x8000
	v_mov_b32_e32 v149, v115
	s_addc_u32 s39, s63, 0
	s_add_i32 s86, s37, 0x8000
	v_mov_b32_e32 v153, v115
	global_load_lds_dwordx4 v[8:9], off
	v_lshl_add_u64 v[8:9], s[38:39], 0, v[148:149]
	s_mov_b32 m0, s86
	s_add_i32 s87, s37, 0xa000
	global_load_lds_dwordx4 v[8:9], off
	v_lshl_add_u64 v[8:9], s[38:39], 0, v[152:153]
	s_add_u32 s38, s64, 0x9000
	s_mov_b32 m0, s87
	s_addc_u32 s39, s65, 0
	global_load_lds_dwordx4 v[8:9], off
	s_add_i32 m0, s37, 0x1c000
	v_lshl_add_u64 v[8:9], s[38:39], 0, v[150:151]
	global_load_lds_dwordx4 v[8:9], off
	v_lshl_add_u64 v[8:9], s[38:39], 0, v[154:155]
	s_add_i32 m0, s37, 0x1e000
	s_cmpk_lt_u32 s15, 0x100
	global_load_lds_dwordx4 v[8:9], off
	v_or_b32_e32 v8, 16, v1
	v_lshlrev_b32_e32 v17, 4, v8
	v_or_b32_e32 v9, 32, v1
	v_lshlrev_b32_e32 v8, 2, v8
	v_or_b32_e32 v19, 48, v1
	v_bitop3_b32 v29, v8, 1, s16 bitop3:0x36
	v_lshlrev_b32_e32 v8, 2, v9
	s_cselect_b64 s[48:49], -1, 0
	v_add_u32_e32 v21, 0x80, v1
	v_bitop3_b32 v30, v8, 1, s16 bitop3:0x36
	v_lshlrev_b32_e32 v8, 2, v19
	s_lshl_b32 s15, s50, 8
	v_lshlrev_b32_e32 v20, 4, v19
	v_add_u32_e32 v23, 0x90, v1
	s_bfe_u32 s88, s50, 0x10001
	v_bitop3_b32 v19, v8, 1, s16 bitop3:0x36
	v_lshlrev_b32_e32 v8, 2, v21
	s_and_b32 s15, s15, 0x100
	v_lshlrev_b32_e32 v22, 4, v21
	v_add_u32_e32 v25, 0xa0, v1
	v_bitop3_b32 v21, v8, 1, s16 bitop3:0x36
	v_lshlrev_b32_e32 v8, 2, v23
	s_add_u32 s42, s42, s15
	v_lshlrev_b32_e32 v24, 4, v23
	v_add_u32_e32 v27, 0xb0, v1
	v_bitop3_b32 v23, v8, 1, s16 bitop3:0x36
	v_lshlrev_b32_e32 v8, 2, v25
	s_addc_u32 s43, s43, 0
	v_lshlrev_b32_e32 v26, 4, v25
	v_bitop3_b32 v25, v8, 1, s16 bitop3:0x36
	v_lshlrev_b32_e32 v8, 2, v27
	v_lshlrev_b32_e32 v114, 5, v10
	s_cmp_lg_u64 s[46:47], 0
	v_lshlrev_b32_e32 v18, 4, v9
	v_lshlrev_b32_e32 v28, 4, v27
	v_bitop3_b32 v27, v8, 1, s16 bitop3:0x36
	v_lshl_add_u64 v[8:9], s[42:43], 0, v[114:115]
	s_mov_b64 s[26:27], 0x36100000
	s_cselect_b64 s[50:51], -1, 0
	s_mov_b64 s[42:43], 0x3e104000
	s_abs_i32 s89, s4
	v_lshl_add_u64 v[166:167], v[8:9], 0, s[26:27]
	v_lshl_add_u64 v[168:169], v[8:9], 0, s[42:43]
	v_cvt_f32_u32_e32 v8, s89
	v_lshlrev_b32_e32 v12, 3, v10
	v_cmp_eq_u32_e64 s[40:41], 0, v11
	v_bitop3_b32 v11, v13, 1, s16 bitop3:0x36
	v_rcp_iflag_f32_e32 v8, v8
	s_lshl_b32 s15, s16, 2
	v_lshl_or_b32 v209, s16, 6, v12
	v_readlane_b32 s17, v255, 5
	v_mul_f32_e32 v8, 0x4f7ffffe, v8
	v_cvt_u32_f32_e32 v8, v8
	v_lshlrev_b32_e32 v16, 4, v1
	s_add_i32 s15, s17, s15
	v_add_u32_e32 v183, s15, v16
	v_readfirstlane_b32 s16, v8
	v_lshlrev_b32_e32 v8, 10, v2
	v_and_b32_e32 v8, 0xfffff800, v8
	v_lshl_add_u32 v3, v3, 7, v8
	v_and_b32_e32 v2, 1, v2
	v_add_u32_e32 v195, s15, v17
	v_add_u32_e32 v197, s15, v18
	v_add_u32_e32 v199, s15, v20
	v_add_u32_e32 v201, s15, v22
	v_add_u32_e32 v203, s15, v24
	v_add_u32_e32 v205, s15, v26
	v_add_u32_e32 v207, s15, v28
	s_sub_i32 s15, 0, s89
	v_lshl_or_b32 v2, v2, 6, v3
	s_mul_i32 s15, s15, s16
	v_lshl_add_u32 v170, v4, 1, v2
	v_lshlrev_b32_e32 v2, 10, v5
	s_mul_hi_u32 s15, s16, s15
	v_and_b32_e32 v2, 0xfffff800, v2
	s_waitcnt vmcnt(8)
	s_barrier
	s_waitcnt vmcnt(6)
	s_add_i32 s93, s16, s15
	s_lshl_b32 s15, s8, 8
	v_readlane_b32 s16, v255, 4
	v_lshl_add_u32 v2, v6, 7, v2
	v_and_b32_e32 v3, 1, v5
	s_add_i32 s15, s16, s15
	v_lshl_or_b32 v2, v3, 6, v2
	s_mov_b32 s14, 0
	v_cmp_eq_u32_e64 s[38:39], 0, v10
	v_lshl_add_u32 v194, v11, 2, s17
	v_lshl_add_u32 v196, v29, 2, s17
	v_lshl_add_u32 v198, v30, 2, s17
	v_lshl_add_u32 v200, v19, 2, s17
	v_lshl_add_u32 v202, v21, 2, s17
	v_lshl_add_u32 v204, v23, 2, s17
	v_lshl_add_u32 v206, v25, 2, s17
	v_lshl_add_u32 v208, v27, 2, s17
	s_ashr_i32 s92, s4, 31
	v_add_u32_e32 v210, s15, v15
	v_add_u32_e32 v211, s16, v13
	v_mov_b32_e32 v171, v115
	v_lshl_add_u32 v172, v7, 1, v2
	v_mov_b32_e32 v173, v115
	v_add_u32_e32 v212, 0, v14
	s_mov_b32 s94, 0
	s_barrier
	s_branch .LBB0_168

.LBB0_336:
	s_and_b32 s16, s37, 3
	s_lshl_b32 s17, s15, 13
	s_lshl_b32 s29, s16, 12
	s_add_u32 s37, s44, 0x1a100000
	s_addc_u32 s64, s45, 0
	s_add_u32 s42, s44, 0x22100000
	s_addc_u32 s43, s45, 0
	s_add_u32 s44, s44, 0x3e102000
	s_addc_u32 s45, s45, 0
	s_add_u32 s38, s58, 0x8000
	v_mov_b32_e32 v143, v115
	s_addc_u32 s39, s59, 0
	s_add_i32 m0, s13, 0x18000
	v_lshl_add_u64 v[10:11], s[38:39], 0, v[142:143]
	v_mov_b32_e32 v147, v115
	global_load_lds_dwordx4 v[10:11], off
	s_add_i32 m0, s13, 0x1a000
	v_lshl_add_u64 v[10:11], s[38:39], 0, v[146:147]
	s_add_u32 s38, s56, 0x8000
	v_mov_b32_e32 v141, v115
	s_addc_u32 s39, s57, 0
	s_add_i32 s65, s13, 0x8000
	v_mov_b32_e32 v145, v115
	global_load_lds_dwordx4 v[10:11], off
	v_lshl_add_u64 v[10:11], s[38:39], 0, v[140:141]
	s_mov_b32 m0, s65
	s_add_i32 s66, s13, 0xa000
	global_load_lds_dwordx4 v[10:11], off
	v_lshl_add_u64 v[10:11], s[38:39], 0, v[144:145]
	s_add_u32 s38, s58, 0x9000
	s_mov_b32 m0, s66
	s_addc_u32 s39, s59, 0
	global_load_lds_dwordx4 v[10:11], off
	s_add_i32 m0, s13, 0x1c000
	v_lshl_add_u64 v[10:11], s[38:39], 0, v[142:143]
	global_load_lds_dwordx4 v[10:11], off
	v_lshl_add_u64 v[10:11], s[38:39], 0, v[146:147]
	s_add_i32 m0, s13, 0x1e000
	v_and_b32_e32 v9, 15, v2
	global_load_lds_dwordx4 v[10:11], off
	v_lshrrev_b32_e32 v2, 1, v2
	v_and_b32_e32 v2, 24, v2
	v_lshlrev_b32_e32 v10, 1, v2
	v_lshl_or_b32 v173, s16, 6, v2
	v_lshlrev_b32_e32 v2, 10, v3
	v_and_b32_e32 v2, 0xfffff800, v2
	v_lshl_add_u32 v2, v4, 7, v2
	v_and_b32_e32 v3, 1, v3
	v_lshl_or_b32 v2, v3, 6, v2
	s_cmpk_lt_u32 s14, 0x100
	v_lshl_add_u32 v148, v5, 1, v2
	v_lshlrev_b32_e32 v2, 10, v6
	v_lshl_or_b32 v1, s15, 6, v9
	v_lshl_or_b32 v10, v9, 6, v10
	v_lshlrev_b32_e32 v9, 2, v9
	s_cselect_b64 s[46:47], -1, 0
	s_lshl_b32 s14, s15, 8
	v_and_b32_e32 v2, 0xfffff800, v2
	v_and_b32_e32 v11, 32, v9
	s_waitcnt vmcnt(8)
	s_barrier
	s_waitcnt vmcnt(6)
	s_add_i32 s14, s14, 0
	v_lshl_add_u32 v2, v7, 7, v2
	v_and_b32_e32 v3, 1, v6
	v_bitop3_b32 v12, v10, s17, v11 bitop3:0xde
	s_add_i32 s14, s14, 0x20400
	v_lshl_or_b32 v2, v3, 6, v2
	v_bitop3_b32 v172, v10, s29, v11 bitop3:0xde
	v_add_u32_e32 v174, s14, v9
	v_mov_b32_e32 v149, v115
	v_lshl_add_u32 v150, v8, 1, v2
	v_mov_b32_e32 v151, v115
	s_mov_b32 s14, 0
	v_add_u32_e32 v175, 0, v12
	s_mov_b32 s67, 0
	s_barrier
	s_mov_b32 s32, 0
	s_branch .LBB0_339

.LBB0_493:
	s_and_b32 s16, s24, 3
	s_lshl_b32 s17, s15, 13
	s_lshl_b32 s29, s16, 12
	s_add_u32 s24, s50, 0x1a100000
	s_addc_u32 s37, s51, 0
	s_add_u32 s26, s50, 0x22100000
	s_addc_u32 s27, s51, 0
	s_add_u32 s42, s50, 0x3e100000
	s_addc_u32 s43, s51, 0
	s_add_u32 s38, s56, 0x8000
	v_mov_b32_e32 v143, v115
	s_addc_u32 s39, s57, 0
	s_add_i32 m0, s12, 0x18000
	v_lshl_add_u64 v[10:11], s[38:39], 0, v[142:143]
	v_mov_b32_e32 v147, v115
	global_load_lds_dwordx4 v[10:11], off
	s_add_i32 m0, s12, 0x1a000
	v_lshl_add_u64 v[10:11], s[38:39], 0, v[146:147]
	s_add_u32 s38, s54, 0x8000
	v_mov_b32_e32 v141, v115
	s_addc_u32 s39, s55, 0
	s_add_i32 s62, s12, 0x8000
	v_mov_b32_e32 v145, v115
	global_load_lds_dwordx4 v[10:11], off
	v_lshl_add_u64 v[10:11], s[38:39], 0, v[140:141]
	s_mov_b32 m0, s62
	s_add_i32 s63, s12, 0xa000
	global_load_lds_dwordx4 v[10:11], off
	v_lshl_add_u64 v[10:11], s[38:39], 0, v[144:145]
	s_add_u32 s38, s56, 0x9000
	s_mov_b32 m0, s63
	s_addc_u32 s39, s57, 0
	global_load_lds_dwordx4 v[10:11], off
	s_add_i32 m0, s12, 0x1c000
	v_lshl_add_u64 v[10:11], s[38:39], 0, v[142:143]
	global_load_lds_dwordx4 v[10:11], off
	v_lshl_add_u64 v[10:11], s[38:39], 0, v[146:147]
	s_add_i32 m0, s12, 0x1e000
	v_and_b32_e32 v9, 15, v2
	global_load_lds_dwordx4 v[10:11], off
	v_lshrrev_b32_e32 v2, 1, v2
	v_and_b32_e32 v2, 24, v2
	v_lshlrev_b32_e32 v10, 1, v2
	v_lshl_or_b32 v173, s16, 6, v2
	v_lshlrev_b32_e32 v2, 10, v3
	v_and_b32_e32 v2, 0xfffff800, v2
	v_lshl_add_u32 v2, v4, 7, v2
	v_and_b32_e32 v3, 1, v3
	v_lshl_or_b32 v2, v3, 6, v2
	s_cmpk_lt_u32 s14, 0x100
	v_lshl_add_u32 v148, v5, 1, v2
	v_lshlrev_b32_e32 v2, 10, v6
	v_lshl_or_b32 v1, s15, 6, v9
	v_lshl_or_b32 v10, v9, 6, v10
	v_lshlrev_b32_e32 v9, 2, v9
	s_cselect_b64 s[44:45], -1, 0
	s_lshl_b32 s14, s15, 8
	v_and_b32_e32 v2, 0xfffff800, v2
	v_and_b32_e32 v11, 32, v9
	s_waitcnt vmcnt(8)
	s_barrier
	s_waitcnt vmcnt(6)
	s_add_i32 s14, s14, 0
	v_lshl_add_u32 v2, v7, 7, v2
	v_and_b32_e32 v3, 1, v6
	v_bitop3_b32 v12, v10, s17, v11 bitop3:0xde
	s_add_i32 s14, s14, 0x20400
	v_lshl_or_b32 v2, v3, 6, v2
	v_bitop3_b32 v172, v10, s29, v11 bitop3:0xde
	v_add_u32_e32 v174, s14, v9
	v_mov_b32_e32 v149, v115
	v_lshl_add_u32 v150, v8, 1, v2
	v_mov_b32_e32 v151, v115
	s_mov_b32 s14, 0
	v_add_u32_e32 v175, 0, v12
	s_mov_b32 s64, 0
	s_barrier
	s_mov_b32 s32, 0
	s_branch .LBB0_496

.LBB0_1069:
	v_or_b32_e32 v1, s10, v139
	s_add_u32 s8, s8, 0x36300000
	v_lshlrev_b32_e32 v67, 6, v1
	s_movk_i32 s16, 0x3c0
	v_lshlrev_b32_e32 v68, 2, v1
	s_addc_u32 s9, s9, 0
	v_and_or_b32 v67, v67, s16, v66
	s_lshl_b32 s16, s28, 13
	v_and_b32_e32 v68, 32, v68
	v_bitop3_b32 v150, v67, s16, v68 bitop3:0xde
	v_lshlrev_b32_e32 v67, 2, v139
	v_lshl_or_b32 v66, v139, 6, v66
	s_lshl_b32 s16, s12, 12
	v_and_b32_e32 v67, 32, v67
	v_bitop3_b32 v146, v66, s16, v67 bitop3:0xde
	s_add_u32 s16, s50, 0x8000
	s_addc_u32 s17, s51, 0
	s_add_i32 m0, s20, 0x18000
	v_lshl_add_u64 v[66:67], s[16:17], 0, v[114:115]
	v_mov_b32_e32 v137, v115
	global_load_lds_dwordx4 v[66:67], off
	s_add_i32 m0, s20, 0x1a000
	v_lshl_add_u64 v[66:67], s[16:17], 0, v[136:137]
	s_add_u32 s16, s52, 0x8000
	v_mov_b32_e32 v133, v115
	s_addc_u32 s17, s53, 0
	s_add_i32 s59, s20, 0x8000
	v_mov_b32_e32 v135, v115
	global_load_lds_dwordx4 v[66:67], off
	v_lshl_add_u64 v[66:67], s[16:17], 0, v[132:133]
	s_mov_b32 m0, s59
	s_add_i32 s60, s20, 0xa000
	global_load_lds_dwordx4 v[66:67], off
	v_lshl_add_u64 v[66:67], s[16:17], 0, v[134:135]
	s_add_u32 s16, s50, 0x9000
	s_mov_b32 m0, s60
	s_addc_u32 s17, s51, 0
	global_load_lds_dwordx4 v[66:67], off
	s_add_i32 m0, s20, 0x1c000
	v_lshl_add_u64 v[66:67], s[16:17], 0, v[114:115]
	global_load_lds_dwordx4 v[66:67], off
	v_lshl_add_u64 v[66:67], s[16:17], 0, v[136:137]
	s_add_i32 m0, s20, 0x1e000
	v_lshlrev_b32_e32 v147, 3, v138
	global_load_lds_dwordx4 v[66:67], off
	s_waitcnt vmcnt(8)
	s_barrier
	s_waitcnt vmcnt(6)
	s_barrier
	s_waitcnt vmcnt(6)
	v_lshlrev_b32_e32 v116, 16, v62
	v_and_b32_e32 v117, 0xffff0000, v62
	v_lshlrev_b32_e32 v118, 16, v63
	v_and_b32_e32 v119, 0xffff0000, v63
	v_lshlrev_b32_e32 v124, 16, v64
	v_and_b32_e32 v125, 0xffff0000, v64
	v_lshlrev_b32_e32 v126, 16, v65
	v_and_b32_e32 v127, 0xffff0000, v65
	v_lshlrev_b32_e32 v120, 16, v58
	v_and_b32_e32 v121, 0xffff0000, v58
	v_lshlrev_b32_e32 v122, 16, v59
	v_and_b32_e32 v123, 0xffff0000, v59
	v_lshlrev_b32_e32 v128, 16, v60
	v_and_b32_e32 v129, 0xffff0000, v60
	v_lshlrev_b32_e32 v130, 16, v61
	v_and_b32_e32 v131, 0xffff0000, v61
	v_lshlrev_b32_e32 v98, 16, v54
	v_and_b32_e32 v99, 0xffff0000, v54
	v_lshlrev_b32_e32 v100, 16, v55
	v_and_b32_e32 v101, 0xffff0000, v55
	v_lshlrev_b32_e32 v102, 16, v56
	v_and_b32_e32 v103, 0xffff0000, v56
	v_lshlrev_b32_e32 v104, 16, v57
	v_and_b32_e32 v105, 0xffff0000, v57
	v_lshlrev_b32_e32 v106, 16, v50
	v_and_b32_e32 v107, 0xffff0000, v50
	v_lshlrev_b32_e32 v108, 16, v51
	v_and_b32_e32 v109, 0xffff0000, v51
	v_lshlrev_b32_e32 v110, 16, v52
	v_and_b32_e32 v111, 0xffff0000, v52
	v_lshlrev_b32_e32 v112, 16, v53
	v_and_b32_e32 v113, 0xffff0000, v53
	v_lshlrev_b32_e32 v82, 16, v46
	v_and_b32_e32 v83, 0xffff0000, v46
	v_lshlrev_b32_e32 v84, 16, v47
	v_and_b32_e32 v85, 0xffff0000, v47
	v_lshlrev_b32_e32 v90, 16, v48
	v_and_b32_e32 v91, 0xffff0000, v48
	v_lshlrev_b32_e32 v92, 16, v49
	v_and_b32_e32 v93, 0xffff0000, v49
	v_lshlrev_b32_e32 v86, 16, v42
	v_and_b32_e32 v87, 0xffff0000, v42
	v_lshlrev_b32_e32 v88, 16, v43
	v_and_b32_e32 v89, 0xffff0000, v43
	v_lshlrev_b32_e32 v94, 16, v44
	v_and_b32_e32 v95, 0xffff0000, v44
	v_lshlrev_b32_e32 v96, 16, v45
	v_and_b32_e32 v97, 0xffff0000, v45
	v_lshlrev_b32_e32 v58, 16, v38
	v_and_b32_e32 v59, 0xffff0000, v38
	v_lshlrev_b32_e32 v60, 16, v39
	v_and_b32_e32 v61, 0xffff0000, v39
	v_lshlrev_b32_e32 v70, 16, v40
	v_and_b32_e32 v71, 0xffff0000, v40
	v_lshlrev_b32_e32 v72, 16, v41
	v_and_b32_e32 v73, 0xffff0000, v41
	v_lshlrev_b32_e32 v74, 16, v30
	v_and_b32_e32 v75, 0xffff0000, v30
	v_lshlrev_b32_e32 v76, 16, v31
	v_and_b32_e32 v77, 0xffff0000, v31
	v_lshlrev_b32_e32 v78, 16, v32
	v_and_b32_e32 v79, 0xffff0000, v32
	v_lshlrev_b32_e32 v80, 16, v33
	v_and_b32_e32 v81, 0xffff0000, v33
	v_lshlrev_b32_e32 v50, 16, v34
	v_and_b32_e32 v51, 0xffff0000, v34
	v_lshlrev_b32_e32 v52, 16, v35
	v_and_b32_e32 v53, 0xffff0000, v35
	v_lshlrev_b32_e32 v62, 16, v36
	v_and_b32_e32 v63, 0xffff0000, v36
	v_lshlrev_b32_e32 v64, 16, v37
	v_and_b32_e32 v65, 0xffff0000, v37
	v_lshlrev_b32_e32 v54, 16, v26
	v_and_b32_e32 v55, 0xffff0000, v26
	v_lshlrev_b32_e32 v56, 16, v27
	v_and_b32_e32 v57, 0xffff0000, v27
	v_lshlrev_b32_e32 v66, 16, v28
	v_and_b32_e32 v67, 0xffff0000, v28
	v_lshlrev_b32_e32 v68, 16, v29
	v_and_b32_e32 v69, 0xffff0000, v29
	v_lshlrev_b32_e32 v34, 16, v22
	v_and_b32_e32 v35, 0xffff0000, v22
	v_lshlrev_b32_e32 v36, 16, v23
	v_and_b32_e32 v37, 0xffff0000, v23
	v_lshlrev_b32_e32 v38, 16, v24
	v_and_b32_e32 v39, 0xffff0000, v24
	v_lshlrev_b32_e32 v40, 16, v25
	v_and_b32_e32 v41, 0xffff0000, v25
	v_lshlrev_b32_e32 v42, 16, v18
	v_and_b32_e32 v43, 0xffff0000, v18
	v_lshlrev_b32_e32 v44, 16, v19
	v_and_b32_e32 v45, 0xffff0000, v19
	v_lshlrev_b32_e32 v46, 16, v20
	v_and_b32_e32 v47, 0xffff0000, v20
	v_lshlrev_b32_e32 v48, 16, v21
	v_and_b32_e32 v49, 0xffff0000, v21
	v_lshlrev_b32_e32 v18, 16, v10
	v_and_b32_e32 v19, 0xffff0000, v10
	v_lshlrev_b32_e32 v20, 16, v11
	v_and_b32_e32 v21, 0xffff0000, v11
	v_lshlrev_b32_e32 v26, 16, v12
	v_and_b32_e32 v27, 0xffff0000, v12
	v_lshlrev_b32_e32 v28, 16, v13
	v_and_b32_e32 v29, 0xffff0000, v13
	v_lshlrev_b32_e32 v22, 16, v2
	v_and_b32_e32 v23, 0xffff0000, v2
	v_lshlrev_b32_e32 v24, 16, v3
	v_and_b32_e32 v25, 0xffff0000, v3
	v_lshlrev_b32_e32 v30, 16, v4
	v_and_b32_e32 v31, 0xffff0000, v4
	v_lshlrev_b32_e32 v32, 16, v5
	v_and_b32_e32 v33, 0xffff0000, v5
	v_lshlrev_b32_e32 v2, 16, v6
	v_and_b32_e32 v3, 0xffff0000, v6
	v_lshlrev_b32_e32 v4, 16, v7
	v_and_b32_e32 v5, 0xffff0000, v7
	v_lshlrev_b32_e32 v6, 16, v8
	v_and_b32_e32 v7, 0xffff0000, v8
	v_lshlrev_b32_e32 v8, 16, v9
	v_and_b32_e32 v9, 0xffff0000, v9
	v_lshlrev_b32_e32 v10, 16, v14
	v_and_b32_e32 v11, 0xffff0000, v14
	v_lshlrev_b32_e32 v12, 16, v15
	v_and_b32_e32 v13, 0xffff0000, v15
	v_lshlrev_b32_e32 v14, 16, v16
	v_and_b32_e32 v15, 0xffff0000, v16
	v_lshlrev_b32_e32 v16, 16, v17
	v_and_b32_e32 v17, 0xffff0000, v17
	v_mov_b32_e32 v149, s11
	v_or_b32_e32 v148, s10, v139
	v_cmp_eq_u32_e64 s[38:39], 0, v138
	v_lshlrev_b64 v[138:139], 7, v[148:149]
	v_lshlrev_b32_e32 v148, 1, v147
	v_lshlrev_b32_e32 v147, 10, v140
	v_and_b32_e32 v147, 0xfffff800, v147
	v_lshl_add_u32 v141, v141, 7, v147
	v_and_b32_e32 v140, 1, v140
	v_lshl_or_b32 v140, v140, 6, v141
	v_lshl_add_u32 v140, v142, 1, v140
	v_lshlrev_b32_e32 v142, 10, v143
	v_and_b32_e32 v142, 0xfffff800, v142
	v_lshl_add_u32 v142, v144, 7, v142
	v_and_b32_e32 v143, 1, v143
	s_cmpk_lt_u32 s24, 0x100
	v_lshl_add_u64 v[138:139], s[26:27], 0, v[138:139]
	v_mov_b32_e32 v149, v115
	v_lshl_or_b32 v142, v143, 6, v142
	s_cselect_b64 s[10:11], -1, 0
	s_mov_b32 s61, 0
	s_ashr_i32 s62, s7, 31
	v_lshl_add_u64 v[138:139], v[138:139], 0, v[148:149]
	v_mov_b32_e32 v141, v115
	v_lshl_add_u32 v142, v145, 1, v142
	v_mov_b32_e32 v143, v115
	v_add_u32_e32 v147, 0, v150
	s_branch .LBB0_1072

.LBB0_1220:
	v_and_b32_e32 v9, 15, v1
	v_and_b32_e32 v8, 48, v1
	v_lshlrev_b32_e32 v12, 2, v9
	s_sext_i32_i8 s58, s10
	s_and_b32 s45, s29, 3
	v_lshl_or_b32 v1, v9, 6, v8
	s_lshl_b32 s10, s28, 13
	v_and_b32_e32 v10, 32, v12
	s_lshl_b32 s29, s28, 6
	v_bitop3_b32 v13, v1, s10, v10 bitop3:0xde
	s_lshl_b32 s10, s45, 12
	s_add_u32 s16, s48, 0x8000
	s_addc_u32 s17, s49, 0
	v_bitop3_b32 v1, v1, s10, v10 bitop3:0xde
	s_add_i32 m0, s20, 0x18000
	v_lshl_add_u64 v[10:11], s[16:17], 0, v[114:115]
	v_mov_b32_e32 v137, v115
	global_load_lds_dwordx4 v[10:11], off
	s_add_i32 m0, s20, 0x1a000
	v_lshl_add_u64 v[10:11], s[16:17], 0, v[136:137]
	s_add_u32 s16, s46, 0x8000
	v_mov_b32_e32 v133, v115
	s_addc_u32 s17, s47, 0
	s_add_i32 s54, s20, 0x8000
	v_mov_b32_e32 v135, v115
	global_load_lds_dwordx4 v[10:11], off
	v_lshl_add_u64 v[10:11], s[16:17], 0, v[132:133]
	s_mov_b32 m0, s54
	s_add_i32 s55, s20, 0xa000
	global_load_lds_dwordx4 v[10:11], off
	v_lshl_add_u64 v[10:11], s[16:17], 0, v[134:135]
	s_add_u32 s16, s48, 0x9000
	s_mov_b32 m0, s55
	s_addc_u32 s17, s49, 0
	global_load_lds_dwordx4 v[10:11], off
	s_add_i32 m0, s20, 0x1c000
	v_lshl_add_u64 v[10:11], s[16:17], 0, v[114:115]
	global_load_lds_dwordx4 v[10:11], off
	v_lshl_add_u64 v[10:11], s[16:17], 0, v[136:137]
	s_add_i32 m0, s20, 0x1e000
	s_cmpk_lt_u32 s11, 0x100
	global_load_lds_dwordx4 v[10:11], off
	s_cselect_b64 s[10:11], -1, 0
	s_ashr_i32 s16, s29, 31
	v_or_b32_e32 v10, s29, v9
	v_mov_b32_e32 v11, s16
	v_lshlrev_b64 v[10:11], 7, v[10:11]
	v_lshl_add_u64 v[10:11], s[26:27], 0, v[10:11]
	v_mov_b32_e32 v9, v115
	v_lshl_add_u64 v[8:9], v[10:11], 0, v[8:9]
	s_mov_b64 s[16:17], 0x28100000
	v_lshl_add_u64 v[138:139], v[8:9], 0, s[16:17]
	v_lshlrev_b32_e32 v8, 10, v2
	v_and_b32_e32 v8, 0xfffff800, v8
	v_lshl_add_u32 v3, v3, 7, v8
	v_and_b32_e32 v2, 1, v2
	v_lshl_or_b32 v2, v2, 6, v3
	v_lshl_add_u32 v140, v4, 1, v2
	v_lshlrev_b32_e32 v2, 10, v5
	s_lshl_b32 s16, s28, 8
	v_and_b32_e32 v2, 0xfffff800, v2
	s_waitcnt vmcnt(8)
	s_barrier
	s_waitcnt vmcnt(6)
	s_add_i32 s16, s16, 0
	v_lshl_add_u32 v2, v6, 7, v2
	v_and_b32_e32 v3, 1, v5
	s_add_i32 s16, s16, 0x20400
	v_lshl_or_b32 v2, v3, 6, v2
	v_add_u32_e32 v146, s16, v12
	v_mov_b32_e32 v141, v115
	v_lshl_add_u32 v142, v7, 1, v2
	v_mov_b32_e32 v143, v115
	s_mov_b32 s59, 0
	v_add_u32_e32 v147, 0, v13
	s_mov_b32 s56, 0
	s_barrier
	s_mov_b32 s32, 0
	s_branch .LBB0_1223

.LBB0_1324:
	v_or_b32_e32 v1, s10, v139
	s_add_u32 s8, s8, 0x36300000
	v_lshlrev_b32_e32 v67, 6, v1
	s_movk_i32 s16, 0x3c0
	v_lshlrev_b32_e32 v68, 2, v1
	s_addc_u32 s9, s9, 0
	v_and_or_b32 v67, v67, s16, v66
	s_lshl_b32 s16, s26, 13
	v_and_b32_e32 v68, 32, v68
	v_bitop3_b32 v150, v67, s16, v68 bitop3:0xde
	v_lshlrev_b32_e32 v67, 2, v139
	v_lshl_or_b32 v66, v139, 6, v66
	s_lshl_b32 s16, s14, 12
	v_and_b32_e32 v67, 32, v67
	v_bitop3_b32 v146, v66, s16, v67 bitop3:0xde
	s_add_u32 s16, s50, 0x8000
	s_addc_u32 s17, s51, 0
	s_add_i32 m0, s37, 0x18000
	v_lshl_add_u64 v[66:67], s[16:17], 0, v[114:115]
	v_mov_b32_e32 v137, v115
	global_load_lds_dwordx4 v[66:67], off
	s_add_i32 m0, s37, 0x1a000
	v_lshl_add_u64 v[66:67], s[16:17], 0, v[136:137]
	s_add_u32 s16, s52, 0x8000
	v_mov_b32_e32 v133, v115
	s_addc_u32 s17, s53, 0
	s_add_i32 s61, s37, 0x8000
	v_mov_b32_e32 v135, v115
	global_load_lds_dwordx4 v[66:67], off
	v_lshl_add_u64 v[66:67], s[16:17], 0, v[132:133]
	s_mov_b32 m0, s61
	s_add_i32 s62, s37, 0xa000
	global_load_lds_dwordx4 v[66:67], off
	v_lshl_add_u64 v[66:67], s[16:17], 0, v[134:135]
	s_add_u32 s16, s50, 0x9000
	s_mov_b32 m0, s62
	s_addc_u32 s17, s51, 0
	global_load_lds_dwordx4 v[66:67], off
	s_add_i32 m0, s37, 0x1c000
	v_lshl_add_u64 v[66:67], s[16:17], 0, v[114:115]
	global_load_lds_dwordx4 v[66:67], off
	v_lshl_add_u64 v[66:67], s[16:17], 0, v[136:137]
	s_add_i32 m0, s37, 0x1e000
	v_lshlrev_b32_e32 v147, 3, v138
	global_load_lds_dwordx4 v[66:67], off
	s_waitcnt vmcnt(8)
	s_barrier
	s_waitcnt vmcnt(6)
	s_barrier
	s_waitcnt vmcnt(6)
	v_lshlrev_b32_e32 v116, 16, v62
	v_and_b32_e32 v117, 0xffff0000, v62
	v_lshlrev_b32_e32 v118, 16, v63
	v_and_b32_e32 v119, 0xffff0000, v63
	v_lshlrev_b32_e32 v124, 16, v64
	v_and_b32_e32 v125, 0xffff0000, v64
	v_lshlrev_b32_e32 v126, 16, v65
	v_and_b32_e32 v127, 0xffff0000, v65
	v_lshlrev_b32_e32 v120, 16, v58
	v_and_b32_e32 v121, 0xffff0000, v58
	v_lshlrev_b32_e32 v122, 16, v59
	v_and_b32_e32 v123, 0xffff0000, v59
	v_lshlrev_b32_e32 v128, 16, v60
	v_and_b32_e32 v129, 0xffff0000, v60
	v_lshlrev_b32_e32 v130, 16, v61
	v_and_b32_e32 v131, 0xffff0000, v61
	v_lshlrev_b32_e32 v98, 16, v54
	v_and_b32_e32 v99, 0xffff0000, v54
	v_lshlrev_b32_e32 v100, 16, v55
	v_and_b32_e32 v101, 0xffff0000, v55
	v_lshlrev_b32_e32 v102, 16, v56
	v_and_b32_e32 v103, 0xffff0000, v56
	v_lshlrev_b32_e32 v104, 16, v57
	v_and_b32_e32 v105, 0xffff0000, v57
	v_lshlrev_b32_e32 v106, 16, v50
	v_and_b32_e32 v107, 0xffff0000, v50
	v_lshlrev_b32_e32 v108, 16, v51
	v_and_b32_e32 v109, 0xffff0000, v51
	v_lshlrev_b32_e32 v110, 16, v52
	v_and_b32_e32 v111, 0xffff0000, v52
	v_lshlrev_b32_e32 v112, 16, v53
	v_and_b32_e32 v113, 0xffff0000, v53
	v_lshlrev_b32_e32 v82, 16, v46
	v_and_b32_e32 v83, 0xffff0000, v46
	v_lshlrev_b32_e32 v84, 16, v47
	v_and_b32_e32 v85, 0xffff0000, v47
	v_lshlrev_b32_e32 v90, 16, v48
	v_and_b32_e32 v91, 0xffff0000, v48
	v_lshlrev_b32_e32 v92, 16, v49
	v_and_b32_e32 v93, 0xffff0000, v49
	v_lshlrev_b32_e32 v86, 16, v42
	v_and_b32_e32 v87, 0xffff0000, v42
	v_lshlrev_b32_e32 v88, 16, v43
	v_and_b32_e32 v89, 0xffff0000, v43
	v_lshlrev_b32_e32 v94, 16, v44
	v_and_b32_e32 v95, 0xffff0000, v44
	v_lshlrev_b32_e32 v96, 16, v45
	v_and_b32_e32 v97, 0xffff0000, v45
	v_lshlrev_b32_e32 v58, 16, v38
	v_and_b32_e32 v59, 0xffff0000, v38
	v_lshlrev_b32_e32 v60, 16, v39
	v_and_b32_e32 v61, 0xffff0000, v39
	v_lshlrev_b32_e32 v70, 16, v40
	v_and_b32_e32 v71, 0xffff0000, v40
	v_lshlrev_b32_e32 v72, 16, v41
	v_and_b32_e32 v73, 0xffff0000, v41
	v_lshlrev_b32_e32 v74, 16, v30
	v_and_b32_e32 v75, 0xffff0000, v30
	v_lshlrev_b32_e32 v76, 16, v31
	v_and_b32_e32 v77, 0xffff0000, v31
	v_lshlrev_b32_e32 v78, 16, v32
	v_and_b32_e32 v79, 0xffff0000, v32
	v_lshlrev_b32_e32 v80, 16, v33
	v_and_b32_e32 v81, 0xffff0000, v33
	v_lshlrev_b32_e32 v50, 16, v34
	v_and_b32_e32 v51, 0xffff0000, v34
	v_lshlrev_b32_e32 v52, 16, v35
	v_and_b32_e32 v53, 0xffff0000, v35
	v_lshlrev_b32_e32 v62, 16, v36
	v_and_b32_e32 v63, 0xffff0000, v36
	v_lshlrev_b32_e32 v64, 16, v37
	v_and_b32_e32 v65, 0xffff0000, v37
	v_lshlrev_b32_e32 v54, 16, v26
	v_and_b32_e32 v55, 0xffff0000, v26
	v_lshlrev_b32_e32 v56, 16, v27
	v_and_b32_e32 v57, 0xffff0000, v27
	v_lshlrev_b32_e32 v66, 16, v28
	v_and_b32_e32 v67, 0xffff0000, v28
	v_lshlrev_b32_e32 v68, 16, v29
	v_and_b32_e32 v69, 0xffff0000, v29
	v_lshlrev_b32_e32 v34, 16, v22
	v_and_b32_e32 v35, 0xffff0000, v22
	v_lshlrev_b32_e32 v36, 16, v23
	v_and_b32_e32 v37, 0xffff0000, v23
	v_lshlrev_b32_e32 v38, 16, v24
	v_and_b32_e32 v39, 0xffff0000, v24
	v_lshlrev_b32_e32 v40, 16, v25
	v_and_b32_e32 v41, 0xffff0000, v25
	v_lshlrev_b32_e32 v42, 16, v18
	v_and_b32_e32 v43, 0xffff0000, v18
	v_lshlrev_b32_e32 v44, 16, v19
	v_and_b32_e32 v45, 0xffff0000, v19
	v_lshlrev_b32_e32 v46, 16, v20
	v_and_b32_e32 v47, 0xffff0000, v20
	v_lshlrev_b32_e32 v48, 16, v21
	v_and_b32_e32 v49, 0xffff0000, v21
	v_lshlrev_b32_e32 v18, 16, v10
	v_and_b32_e32 v19, 0xffff0000, v10
	v_lshlrev_b32_e32 v20, 16, v11
	v_and_b32_e32 v21, 0xffff0000, v11
	v_lshlrev_b32_e32 v26, 16, v12
	v_and_b32_e32 v27, 0xffff0000, v12
	v_lshlrev_b32_e32 v28, 16, v13
	v_and_b32_e32 v29, 0xffff0000, v13
	v_lshlrev_b32_e32 v22, 16, v2
	v_and_b32_e32 v23, 0xffff0000, v2
	v_lshlrev_b32_e32 v24, 16, v3
	v_and_b32_e32 v25, 0xffff0000, v3
	v_lshlrev_b32_e32 v30, 16, v4
	v_and_b32_e32 v31, 0xffff0000, v4
	v_lshlrev_b32_e32 v32, 16, v5
	v_and_b32_e32 v33, 0xffff0000, v5
	v_lshlrev_b32_e32 v2, 16, v6
	v_and_b32_e32 v3, 0xffff0000, v6
	v_lshlrev_b32_e32 v4, 16, v7
	v_and_b32_e32 v5, 0xffff0000, v7
	v_lshlrev_b32_e32 v6, 16, v8
	v_and_b32_e32 v7, 0xffff0000, v8
	v_lshlrev_b32_e32 v8, 16, v9
	v_and_b32_e32 v9, 0xffff0000, v9
	v_lshlrev_b32_e32 v10, 16, v14
	v_and_b32_e32 v11, 0xffff0000, v14
	v_lshlrev_b32_e32 v12, 16, v15
	v_and_b32_e32 v13, 0xffff0000, v15
	v_lshlrev_b32_e32 v14, 16, v16
	v_and_b32_e32 v15, 0xffff0000, v16
	v_lshlrev_b32_e32 v16, 16, v17
	v_and_b32_e32 v17, 0xffff0000, v17
	v_mov_b32_e32 v149, s11
	v_or_b32_e32 v148, s10, v139
	v_cmp_eq_u32_e64 s[38:39], 0, v138
	v_lshlrev_b64 v[138:139], 7, v[148:149]
	v_lshlrev_b32_e32 v148, 1, v147
	v_lshlrev_b32_e32 v147, 10, v140
	v_and_b32_e32 v147, 0xfffff800, v147
	v_lshl_add_u32 v141, v141, 7, v147
	v_and_b32_e32 v140, 1, v140
	v_lshl_or_b32 v140, v140, 6, v141
	v_lshl_add_u32 v140, v142, 1, v140
	v_lshlrev_b32_e32 v142, 10, v143
	v_and_b32_e32 v142, 0xfffff800, v142
	v_lshl_add_u32 v142, v144, 7, v142
	v_and_b32_e32 v143, 1, v143
	s_cmpk_lt_u32 s24, 0x100
	v_lshl_add_u64 v[138:139], s[0:1], 0, v[138:139]
	v_mov_b32_e32 v149, v115
	v_lshl_or_b32 v142, v143, 6, v142
	s_cselect_b64 s[10:11], -1, 0
	s_mov_b32 s63, 0
	s_ashr_i32 s64, s7, 31
	v_lshl_add_u64 v[138:139], v[138:139], 0, v[148:149]
	v_mov_b32_e32 v141, v115
	v_lshl_add_u32 v142, v145, 1, v142
	v_mov_b32_e32 v143, v115
	v_add_u32_e32 v147, 0, v150
	s_branch .LBB0_1327

.LBB0_1366:
	v_or_b32_e32 v1, s9, v140
	v_lshlrev_b32_e32 v2, 6, v1
	s_movk_i32 s16, 0x3c0
	v_lshlrev_b32_e32 v3, 2, v1
	v_and_or_b32 v2, v2, s16, v114
	s_lshl_b32 s11, s11, 13
	v_and_b32_e32 v3, 32, v3
	s_ashr_i32 s27, s28, 2
	v_bitop3_b32 v151, v2, s11, v3 bitop3:0xde
	s_lshl_b32 s11, s15, 12
	v_lshlrev_b32_e32 v3, 2, v140
	s_add_u32 s16, s42, 0x8000
	v_mov_b32_e32 v135, v115
	v_lshl_or_b32 v2, v140, 6, v114
	v_and_b32_e32 v3, 32, v3
	s_addc_u32 s17, s43, 0
	v_bitop3_b32 v144, v2, s11, v3 bitop3:0xde
	s_add_i32 m0, s37, 0x18000
	v_lshl_add_u64 v[2:3], s[16:17], 0, v[134:135]
	v_mov_b32_e32 v139, v115
	global_load_lds_dwordx4 v[2:3], off
	s_add_i32 m0, s37, 0x1a000
	v_lshl_add_u64 v[2:3], s[16:17], 0, v[138:139]
	s_add_u32 s16, s44, 0x8000
	v_mov_b32_e32 v133, v115
	s_addc_u32 s17, s45, 0
	s_add_i32 s53, s37, 0x8000
	v_mov_b32_e32 v137, v115
	global_load_lds_dwordx4 v[2:3], off
	v_lshl_add_u64 v[2:3], s[16:17], 0, v[132:133]
	s_mov_b32 m0, s53
	s_add_i32 s54, s37, 0xa000
	global_load_lds_dwordx4 v[2:3], off
	v_lshl_add_u64 v[2:3], s[16:17], 0, v[136:137]
	s_add_u32 s16, s42, 0x9000
	s_mov_b32 m0, s54
	s_addc_u32 s17, s43, 0
	global_load_lds_dwordx4 v[2:3], off
	s_add_i32 m0, s37, 0x1c000
	v_lshl_add_u64 v[2:3], s[16:17], 0, v[134:135]
	global_load_lds_dwordx4 v[2:3], off
	v_lshl_add_u64 v[2:3], s[16:17], 0, v[138:139]
	s_add_i32 m0, s37, 0x1e000
	s_nop 0
	global_load_lds_dwordx4 v[2:3], off
	s_waitcnt vmcnt(8)
	s_barrier
	s_waitcnt vmcnt(6)
	s_barrier
	s_waitcnt vmcnt(6)
	v_lshlrev_b32_e32 v2, 16, v6
	v_and_b32_e32 v3, 0xffff0000, v6
	v_lshlrev_b32_e32 v4, 16, v7
	v_and_b32_e32 v5, 0xffff0000, v7
	v_lshlrev_b32_e32 v6, 16, v8
	v_and_b32_e32 v7, 0xffff0000, v8
	v_lshlrev_b32_e32 v8, 16, v9
	v_and_b32_e32 v9, 0xffff0000, v9
	v_lshlrev_b32_e32 v18, 16, v10
	v_and_b32_e32 v19, 0xffff0000, v10
	v_lshlrev_b32_e32 v20, 16, v11
	v_and_b32_e32 v21, 0xffff0000, v11
	v_lshlrev_b32_e32 v22, 16, v12
	v_and_b32_e32 v23, 0xffff0000, v12
	v_lshlrev_b32_e32 v24, 16, v13
	v_and_b32_e32 v25, 0xffff0000, v13
	v_lshlrev_b32_e32 v10, 16, v14
	v_and_b32_e32 v11, 0xffff0000, v14
	v_lshlrev_b32_e32 v12, 16, v15
	v_and_b32_e32 v13, 0xffff0000, v15
	v_lshlrev_b32_e32 v14, 16, v16
	v_and_b32_e32 v15, 0xffff0000, v16
	v_lshlrev_b32_e32 v16, 16, v17
	v_and_b32_e32 v17, 0xffff0000, v17
	v_lshlrev_b32_e32 v34, 16, v26
	v_and_b32_e32 v35, 0xffff0000, v26
	v_lshlrev_b32_e32 v36, 16, v27
	v_and_b32_e32 v37, 0xffff0000, v27
	v_lshlrev_b32_e32 v38, 16, v28
	v_and_b32_e32 v39, 0xffff0000, v28
	v_lshlrev_b32_e32 v40, 16, v29
	v_and_b32_e32 v41, 0xffff0000, v29
	v_lshlrev_b32_e32 v26, 16, v30
	v_and_b32_e32 v27, 0xffff0000, v30
	v_lshlrev_b32_e32 v28, 16, v31
	v_and_b32_e32 v29, 0xffff0000, v31
	v_lshlrev_b32_e32 v30, 16, v32
	v_and_b32_e32 v31, 0xffff0000, v32
	v_lshlrev_b32_e32 v32, 16, v33
	v_and_b32_e32 v33, 0xffff0000, v33
	v_lshlrev_b32_e32 v50, 16, v42
	v_and_b32_e32 v51, 0xffff0000, v42
	v_lshlrev_b32_e32 v52, 16, v43
	v_and_b32_e32 v53, 0xffff0000, v43
	v_lshlrev_b32_e32 v54, 16, v44
	v_and_b32_e32 v55, 0xffff0000, v44
	v_lshlrev_b32_e32 v56, 16, v45
	v_and_b32_e32 v57, 0xffff0000, v45
	v_lshlrev_b32_e32 v42, 16, v46
	v_and_b32_e32 v43, 0xffff0000, v46
	v_lshlrev_b32_e32 v44, 16, v47
	v_and_b32_e32 v45, 0xffff0000, v47
	v_lshlrev_b32_e32 v46, 16, v48
	v_and_b32_e32 v47, 0xffff0000, v48
	v_lshlrev_b32_e32 v48, 16, v49
	v_and_b32_e32 v49, 0xffff0000, v49
	v_lshlrev_b32_e32 v58, 16, v62
	v_and_b32_e32 v59, 0xffff0000, v62
	v_lshlrev_b32_e32 v60, 16, v63
	v_and_b32_e32 v61, 0xffff0000, v63
	v_lshlrev_b32_e32 v62, 16, v64
	v_and_b32_e32 v63, 0xffff0000, v64
	v_lshlrev_b32_e32 v64, 16, v65
	v_and_b32_e32 v65, 0xffff0000, v65
	v_lshlrev_b32_e32 v66, 16, v70
	v_and_b32_e32 v67, 0xffff0000, v70
	v_lshlrev_b32_e32 v68, 16, v71
	v_and_b32_e32 v69, 0xffff0000, v71
	v_lshlrev_b32_e32 v70, 16, v72
	v_and_b32_e32 v71, 0xffff0000, v72
	v_lshlrev_b32_e32 v72, 16, v73
	v_and_b32_e32 v73, 0xffff0000, v73
	v_lshlrev_b32_e32 v82, 16, v74
	v_and_b32_e32 v83, 0xffff0000, v74
	v_lshlrev_b32_e32 v84, 16, v75
	v_and_b32_e32 v85, 0xffff0000, v75
	v_lshlrev_b32_e32 v90, 16, v76
	v_and_b32_e32 v91, 0xffff0000, v76
	v_lshlrev_b32_e32 v92, 16, v77
	v_and_b32_e32 v93, 0xffff0000, v77
	v_lshlrev_b32_e32 v74, 16, v78
	v_and_b32_e32 v75, 0xffff0000, v78
	v_lshlrev_b32_e32 v76, 16, v79
	v_and_b32_e32 v77, 0xffff0000, v79
	v_lshlrev_b32_e32 v78, 16, v80
	v_and_b32_e32 v79, 0xffff0000, v80
	v_lshlrev_b32_e32 v80, 16, v81
	v_and_b32_e32 v81, 0xffff0000, v81
	v_lshlrev_b32_e32 v98, 16, v86
	v_and_b32_e32 v99, 0xffff0000, v86
	v_lshlrev_b32_e32 v100, 16, v87
	v_and_b32_e32 v101, 0xffff0000, v87
	v_lshlrev_b32_e32 v106, 16, v88
	v_and_b32_e32 v107, 0xffff0000, v88
	v_lshlrev_b32_e32 v108, 16, v89
	v_and_b32_e32 v109, 0xffff0000, v89
	v_lshlrev_b32_e32 v86, 16, v94
	v_and_b32_e32 v87, 0xffff0000, v94
	v_lshlrev_b32_e32 v88, 16, v95
	v_and_b32_e32 v89, 0xffff0000, v95
	v_lshlrev_b32_e32 v94, 16, v96
	v_and_b32_e32 v95, 0xffff0000, v96
	v_lshlrev_b32_e32 v96, 16, v97
	v_and_b32_e32 v97, 0xffff0000, v97
	v_lshlrev_b32_e32 v116, 16, v102
	v_and_b32_e32 v117, 0xffff0000, v102
	v_lshlrev_b32_e32 v118, 16, v103
	v_and_b32_e32 v119, 0xffff0000, v103
	v_lshlrev_b32_e32 v120, 16, v104
	v_and_b32_e32 v121, 0xffff0000, v104
	v_lshlrev_b32_e32 v122, 16, v105
	v_and_b32_e32 v123, 0xffff0000, v105
	v_lshlrev_b32_e32 v102, 16, v110
	v_and_b32_e32 v103, 0xffff0000, v110
	v_lshlrev_b32_e32 v104, 16, v111
	v_and_b32_e32 v105, 0xffff0000, v111
	v_lshlrev_b32_e32 v110, 16, v112
	v_and_b32_e32 v111, 0xffff0000, v112
	v_lshlrev_b32_e32 v112, 16, v113
	v_and_b32_e32 v113, 0xffff0000, v113
	v_lshlrev_b32_e32 v124, 16, v128
	v_and_b32_e32 v125, 0xffff0000, v128
	v_lshlrev_b32_e32 v126, 16, v129
	v_and_b32_e32 v127, 0xffff0000, v129
	v_lshlrev_b32_e32 v128, 16, v130
	v_and_b32_e32 v129, 0xffff0000, v130
	v_lshlrev_b32_e32 v130, 16, v131
	v_and_b32_e32 v131, 0xffff0000, v131
	v_mov_b32_e32 v141, s10
	v_or_b32_e32 v140, s9, v140
	v_lshlrev_b64 v[140:141], 7, v[140:141]
	v_lshl_add_u64 v[140:141], s[0:1], 0, v[140:141]
	v_lshl_add_u64 v[140:141], v[140:141], 0, v[114:115]
	v_lshlrev_b32_e32 v114, 10, v143
	v_and_b32_e32 v114, 0xfffff800, v114
	v_lshl_or_b32 v145, s15, 6, v142
	v_lshl_add_u32 v114, v146, 7, v114
	v_and_b32_e32 v142, 1, v143
	v_lshl_or_b32 v114, v142, 6, v114
	v_lshlrev_b32_e32 v142, 10, v148
	v_and_b32_e32 v142, 0xfffff800, v142
	v_lshl_add_u32 v142, v149, 7, v142
	v_and_b32_e32 v143, 1, v148
	s_cmpk_lt_u32 s8, 0x100
	v_lshl_or_b32 v142, v143, 6, v142
	s_cselect_b64 s[8:9], -1, 0
	v_lshl_add_u32 v114, v147, 1, v114
	v_lshl_add_u32 v142, v150, 1, v142
	v_mov_b32_e32 v143, v115
	s_mov_b32 s55, 0
	v_add_u32_e32 v146, 0, v151
	s_branch .LBB0_1369
